# speedup vs baseline: 1.0091x; 1.0091x over previous
_Z11prep_kernelPKfS0_S0_PdPtS2_:
	s_bfe_u32 s17, s2, 0x20001
	s_and_b32 s18, s2, 1
	s_lshr_b32 s2, s2, 3
	s_lshl_b32 s17, s17, 6
	s_lshl_b32 s18, s18, 5
	s_or_b32 s2, s2, s17
	s_or_b32 s2, s2, s18
	s_load_dwordx2 s[6:7], s[0:1], 0x0
	s_ashr_i32 s4, s2, 6
	s_and_b32 s12, s2, 63
	s_ashr_i32 s5, s4, 31
	s_lshl_b32 s3, s12, 8
	s_waitcnt lgkmcnt(0)
	s_add_u32 s6, s6, s3
	v_lshlrev_b32_e32 v1, 4, v0
	s_addc_u32 s7, s7, 0
	v_and_b32_e32 v2, 0xf0, v1
	v_mov_b32_e32 v3, 0
	v_lshlrev_b32_e32 v1, 10, v0
	v_lshl_add_u64 v[2:3], s[6:7], 0, v[2:3]
	s_lshl_b64 s[6:7], s[4:5], 22
	v_and_b32_e32 v1, 0xfc000, v1
	v_or_b32_e32 v4, s6, v1
	v_mov_b32_e32 v5, s7
	v_lshl_add_u64 v[2:3], v[2:3], 0, v[4:5]
	s_mov_b32 s3, 0x100000
	v_add_co_u32_e32 v4, vcc, s3, v2
	s_movk_i32 s3, 0x80
	s_nop 0
	v_addc_co_u32_e32 v5, vcc, 0, v3, vcc
	v_add_co_u32_e32 v18, vcc, 0x200000, v2
	global_load_dwordx4 v[14:17], v[2:3], off
	global_load_dwordx4 v[10:13], v[4:5], off
	v_addc_co_u32_e32 v19, vcc, 0, v3, vcc
	v_add_co_u32_e32 v20, vcc, 0x300000, v2
	s_nop 1
	v_addc_co_u32_e32 v21, vcc, 0, v3, vcc
	global_load_dwordx4 v[6:9], v[18:19], off
	global_load_dwordx4 v[2:5], v[20:21], off
	v_cmp_gt_u32_e32 vcc, s3, v0
	s_and_saveexec_b64 s[6:7], vcc
	s_cbranch_execz .LBB0_6
	s_load_dwordx2 s[8:9], s[0:1], 0x28
	v_lshl_or_b32 v1, s2, 7, v0
	v_ashrrev_i32_e32 v24, 5, v1
	v_and_b32_e32 v18, 31, v0
	s_movk_i32 s3, 0x2ff
	v_bfe_u32 v28, v0, 1, 4
	v_cmp_lt_i32_e32 vcc, s3, v24
	v_lshlrev_b32_e32 v22, 5, v18
	s_and_saveexec_b64 s[10:11], vcc
	s_xor_b64 s[10:11], exec, s[10:11]
	s_cbranch_execz .LBB0_3
	s_load_dwordx2 s[14:15], s[0:1], 0x10
	v_add_u32_e32 v18, 0xfffffd00, v24
	v_mov_b32_e32 v19, 0
	v_lshlrev_b64 v[20:21], 10, v[18:19]
	v_mov_b32_e32 v23, v19
	s_waitcnt lgkmcnt(0)
	v_lshl_add_u64 v[20:21], s[14:15], 0, v[20:21]
	v_lshrrev_b32_e32 v18, 1, v18
	s_mov_b32 s3, 0x7ffffff0
	v_lshl_add_u64 v[20:21], v[20:21], 0, v[22:23]
	v_and_or_b32 v18, v18, s3, v28

	.amdhsa_kernel _Z11prep_kernelPKfS0_S0_PdPtS2_
		.amdhsa_group_segment_fixed_size 512
		.amdhsa_private_segment_fixed_size 0
		.amdhsa_kernarg_size 48
		.amdhsa_user_sgpr_count 2
		.amdhsa_user_sgpr_dispatch_ptr 0
		.amdhsa_user_sgpr_queue_ptr 0
		.amdhsa_user_sgpr_kernarg_segment_ptr 1
		.amdhsa_user_sgpr_dispatch_id 0
		.amdhsa_user_sgpr_kernarg_preload_length 0
		.amdhsa_user_sgpr_kernarg_preload_offset 0
		.amdhsa_user_sgpr_private_segment_size 0
		.amdhsa_uses_dynamic_stack 0
		.amdhsa_enable_private_segment 0
		.amdhsa_system_sgpr_workgroup_id_x 1
		.amdhsa_system_sgpr_workgroup_id_y 0
		.amdhsa_system_sgpr_workgroup_id_z 0
		.amdhsa_system_sgpr_workgroup_info 0
		.amdhsa_system_vgpr_workitem_id 0
		.amdhsa_next_free_vgpr 32
		.amdhsa_next_free_sgpr 20
		.amdhsa_accum_offset 32
		.amdhsa_reserve_vcc 1
		.amdhsa_float_round_mode_32 0
		.amdhsa_float_round_mode_16_64 0
		.amdhsa_float_denorm_mode_32 3
		.amdhsa_float_denorm_mode_16_64 3
		.amdhsa_dx10_clamp 1
		.amdhsa_ieee_mode 1
		.amdhsa_fp16_overflow 0
		.amdhsa_tg_split 0
		.amdhsa_exception_fp_ieee_invalid_op 0
		.amdhsa_exception_fp_denorm_src 0
		.amdhsa_exception_fp_ieee_div_zero 0
		.amdhsa_exception_fp_ieee_overflow 0
		.amdhsa_exception_fp_ieee_underflow 0
		.amdhsa_exception_fp_ieee_inexact 0
		.amdhsa_exception_int_div_zero 0
	.end_amdhsa_kernel

_Z10qkv_kernelPKfS0_S0_PKdPKtS0_PhPfS6_:
	s_bfe_u32 s30, s2, 0x20001
	s_and_b32 s31, s2, 1
	s_lshr_b32 s2, s2, 3
	s_lshl_b32 s30, s30, 6
	s_lshl_b32 s31, s31, 5
	s_or_b32 s2, s2, s30
	s_or_b32 s2, s2, s31
	s_load_dwordx2 s[8:9], s[0:1], 0x0
	s_load_dwordx4 s[4:7], s[0:1], 0x18
	s_load_dwordx4 s[20:23], s[0:1], 0x8
	v_lshrrev_b32_e32 v1, 6, v0
	v_and_b32_e32 v146, 63, v0
	v_lshlrev_b32_e32 v134, 14, v1
	v_mov_b32_e32 v135, 0
	s_waitcnt lgkmcnt(0)
	v_lshrrev_b32_e32 v188, 6, v0
	v_and_b32_e32 v189, 31, v0
	v_lshl_add_u32 v188, v188, 5, v189
	v_lshlrev_b32_e32 v188, 2, v188
	global_load_dword v190, v188, s[20:21]
	global_load_dword v191, v188, s[22:23]
	v_lshl_add_u64 v[2:3], s[6:7], 0, v[134:135]
	v_lshlrev_b32_e32 v134, 4, v146
	s_ashr_i32 s6, s2, 6
	v_lshl_add_u64 v[132:133], v[2:3], 0, v[134:135]
	v_lshl_or_b32 v2, s6, 3, v1
	v_ashrrev_i32_e32 v3, 31, v2
	v_lshlrev_b64 v[2:3], 10, v[2:3]
	v_lshl_add_u64 v[2:3], s[4:5], 0, v[2:3]
	v_lshl_add_u64 v[2:3], v[2:3], 0, v[134:135]
	global_load_dwordx4 v[94:97], v[132:133], off
	global_load_dwordx4 v[86:89], v[132:133], off offset:1024
	global_load_dwordx4 v[54:57], v[132:133], off offset:2048
	global_load_dwordx4 v[42:45], v[132:133], off offset:3072
	global_load_dwordx4 v[98:101], v[2:3], off
	s_movk_i32 s7, 0x1000
	v_add_co_u32_e32 v2, vcc, s7, v132
	s_lshl_b32 s3, s2, 6
	s_nop 0
	v_addc_co_u32_e32 v3, vcc, 0, v133, vcc
	s_movk_i32 s4, 0x2000
	v_add_co_u32_e32 v4, vcc, s4, v132
	s_and_b32 s3, s3, 0xfc0
	s_nop 0
	v_addc_co_u32_e32 v5, vcc, 0, v133, vcc
	s_movk_i32 s4, 0x3000
	s_ashr_i32 s7, s6, 31
	s_lshl_b32 s16, s3, 2
	v_add_co_u32_e32 v4, vcc, s4, v132
	v_and_b32_e32 v106, 7, v0
	s_add_u32 s4, s8, s16
	v_addc_co_u32_e32 v5, vcc, 0, v133, vcc
	s_addc_u32 s5, s9, 0
	v_lshlrev_b32_e32 v2, 5, v106
	v_mov_b32_e32 v3, v135
	v_lshrrev_b32_e32 v107, 3, v0
	v_lshl_add_u64 v[2:3], s[4:5], 0, v[2:3]
	s_lshl_b64 s[4:5], s[6:7], 22
	v_lshl_or_b32 v4, v107, 14, s4
	v_mov_b32_e32 v5, s5
	v_lshl_add_u64 v[2:3], v[2:3], 0, v[4:5]
	s_mov_b64 s[4:5], 0x100000
	v_lshl_add_u64 v[4:5], v[2:3], 0, s[4:5]
	s_mov_b32 s4, 0x100000
	v_add_co_u32_e32 v6, vcc, s4, v2
	s_mov_b64 s[4:5], 0x200000
	s_nop 0
	v_addc_co_u32_e32 v7, vcc, 0, v3, vcc
	global_load_dwordx4 v[26:29], v[2:3], off offset:16
	global_load_dwordx4 v[30:33], v[2:3], off
	global_load_dwordx4 v[22:25], v[6:7], off
	global_load_dwordx4 v[18:21], v[4:5], off offset:16
	v_lshl_add_u64 v[4:5], v[2:3], 0, s[4:5]
	s_mov_b32 s4, 0x200000
	v_add_co_u32_e32 v6, vcc, s4, v2
	s_mov_b64 s[4:5], 0x300000
	s_nop 0
	v_addc_co_u32_e32 v7, vcc, 0, v3, vcc
	v_lshl_add_u64 v[102:103], v[2:3], 0, s[4:5]
	s_mov_b32 s4, 0x300000
	v_add_co_u32_e32 v104, vcc, s4, v2
	global_load_dwordx4 v[14:17], v[6:7], off
	global_load_dwordx4 v[10:13], v[4:5], off offset:16
	v_addc_co_u32_e32 v105, vcc, 0, v3, vcc
	global_load_dwordx4 v[6:9], v[104:105], off
	global_load_dwordx4 v[2:5], v[102:103], off offset:16
	s_mov_b64 s[24:25], 0x1000
	s_mov_b64 s[26:27], 0x2000
	s_mov_b64 s[28:29], 0x3000
	v_lshl_add_u64 v[182:183], v[132:133], 0, s[24:25]
	v_lshl_add_u64 v[184:185], v[132:133], 0, s[26:27]
	v_lshl_add_u64 v[186:187], v[132:133], 0, s[28:29]
	global_load_dwordx4 v[78:81], v[182:183], off offset:1024
	global_load_dwordx4 v[82:85], v[182:183], off offset:2048
	global_load_dwordx4 v[74:77], v[182:183], off offset:3072
	global_load_dwordx4 v[90:93], v[184:185], off offset:-4096
	global_load_dwordx4 v[66:69], v[184:185], off
	global_load_dwordx4 v[70:73], v[184:185], off offset:1024
	global_load_dwordx4 v[62:65], v[184:185], off offset:2048
	global_load_dwordx4 v[58:61], v[184:185], off offset:3072
	global_load_dwordx4 v[50:53], v[186:187], off
	global_load_dwordx4 v[46:49], v[186:187], off offset:1024
	global_load_dwordx4 v[38:41], v[186:187], off offset:2048
	global_load_dwordx4 v[34:37], v[186:187], off offset:3072
	v_mbcnt_lo_u32_b32 v102, -1, 0
	v_mbcnt_hi_u32_b32 v108, -1, v102
	v_and_b32_e32 v102, 64, v108
	v_add_u32_e32 v109, 64, v102
	v_xor_b32_e32 v102, 32, v108
	v_cmp_lt_i32_e32 vcc, v102, v109
	s_load_dwordx2 s[8:9], s[0:1], 0x28
	v_cmp_lt_u32_e64 s[4:5], 31, v146
	v_cndmask_b32_e32 v102, v108, v102, vcc
	v_lshlrev_b32_e32 v105, 2, v102
	v_lshlrev_b32_e32 v130, 5, v1
	s_waitcnt vmcnt(20)
	ds_bpermute_b32 v102, v105, v98
	ds_bpermute_b32 v103, v105, v99
	ds_bpermute_b32 v104, v105, v100
	ds_bpermute_b32 v105, v105, v101
	s_waitcnt lgkmcnt(0)
	v_add_f64 v[98:99], v[98:99], v[102:103]
	v_xor_b32_e32 v102, 16, v108
	v_cmp_lt_i32_e32 vcc, v102, v109
	v_add_f64 v[100:101], v[100:101], v[104:105]
	s_nop 0
	v_cndmask_b32_e32 v102, v108, v102, vcc
	v_lshlrev_b32_e32 v141, 2, v102
	ds_bpermute_b32 v102, v141, v98
	ds_bpermute_b32 v103, v141, v99
	ds_bpermute_b32 v104, v141, v100
	ds_bpermute_b32 v105, v141, v101
	s_waitcnt lgkmcnt(2)
	v_add_f64 v[98:99], v[98:99], v[102:103]
	v_xor_b32_e32 v102, 8, v108
	v_cmp_lt_i32_e32 vcc, v102, v109
	s_waitcnt lgkmcnt(0)
	v_add_f64 v[100:101], v[100:101], v[104:105]
	v_cndmask_b32_e32 v102, v108, v102, vcc
	v_lshlrev_b32_e32 v142, 2, v102
	ds_bpermute_b32 v102, v142, v98
	ds_bpermute_b32 v103, v142, v99
	ds_bpermute_b32 v104, v142, v100
	ds_bpermute_b32 v105, v142, v101
	s_waitcnt lgkmcnt(2)
	v_add_f64 v[98:99], v[98:99], v[102:103]
	v_xor_b32_e32 v102, 4, v108
	v_cmp_lt_i32_e32 vcc, v102, v109
	s_waitcnt lgkmcnt(0)
	v_add_f64 v[100:101], v[100:101], v[104:105]
	v_cndmask_b32_e32 v102, v108, v102, vcc
	v_lshlrev_b32_e32 v143, 2, v102
	ds_bpermute_b32 v102, v143, v98
	ds_bpermute_b32 v103, v143, v99
	ds_bpermute_b32 v104, v143, v100
	ds_bpermute_b32 v105, v143, v101
	s_waitcnt lgkmcnt(2)
	v_add_f64 v[98:99], v[98:99], v[102:103]
	v_xor_b32_e32 v102, 2, v108
	v_cmp_lt_i32_e32 vcc, v102, v109
	s_waitcnt lgkmcnt(0)
	v_add_f64 v[100:101], v[100:101], v[104:105]
	v_cndmask_b32_e32 v102, v108, v102, vcc
	v_lshlrev_b32_e32 v144, 2, v102
	ds_bpermute_b32 v102, v144, v98
	ds_bpermute_b32 v103, v144, v99
	ds_bpermute_b32 v104, v144, v100
	ds_bpermute_b32 v105, v144, v101
	s_waitcnt lgkmcnt(2)
	v_add_f64 v[98:99], v[98:99], v[102:103]
	v_xor_b32_e32 v102, 1, v108
	v_cmp_lt_i32_e32 vcc, v102, v109
	s_waitcnt lgkmcnt(0)
	v_add_f64 v[100:101], v[100:101], v[104:105]
	v_cndmask_b32_e32 v102, v108, v102, vcc
	v_lshlrev_b32_e32 v145, 2, v102
	ds_bpermute_b32 v102, v145, v98
	ds_bpermute_b32 v103, v145, v99
	ds_bpermute_b32 v104, v145, v100
	ds_bpermute_b32 v105, v145, v101
	v_cmp_gt_u32_e32 vcc, 32, v146
	s_and_saveexec_b64 s[10:11], s[4:5]
	s_xor_b64 s[4:5], exec, s[10:11]
	v_lshlrev_b32_e32 v130, 5, v1
	s_or_saveexec_b64 s[10:11], s[4:5]
	s_load_dwordx2 s[14:15], s[0:1], 0x38
	s_xor_b64 exec, exec, s[10:11]
	s_cbranch_execz .LBB1_4
	s_load_dwordx4 s[20:23], s[0:1], 0x8
	v_or_b32_e32 v108, v130, v146
	v_lshlrev_b32_e32 v108, 2, v108
	s_waitcnt lgkmcnt(0)
	v_add_f64 v[98:99], v[98:99], v[102:103]
	s_movk_i32 s12, 0xffef
	s_mov_b32 s4, 0
	v_ldexp_f64 v[98:99], v[98:99], s12
	v_add_f64 v[100:101], v[100:101], v[104:105]
	s_mov_b32 s5, 0x3ee00000
	v_mul_f64 v[102:103], v[98:99], v[98:99]
	v_fma_f64 v[100:101], v[100:101], s[4:5], -v[102:103]
	v_cvt_f32_f64_e32 v100, v[100:101]
	s_mov_b32 s13, 0x800000
	v_add_f32_e32 v100, 0x3727c5ac, v100
	v_mul_f32_e32 v101, 0x4b800000, v100
	v_cmp_gt_f32_e64 s[4:5], s13, v100
	v_cvt_f32_f64_e32 v98, v[98:99]
	s_nop 0
	v_cndmask_b32_e64 v100, v100, v101, s[4:5]
	v_rsq_f32_e32 v100, v100
	v_add_u32_e32 v101, 0, v108
	v_mul_f32_e32 v102, 0x45800000, v100
	v_cndmask_b32_e64 v100, v100, v102, s[4:5]
	v_mul_f32_e32 v100, v100, v190
	v_fma_f32 v98, -v100, v98, v191
	ds_write2st64_b32 v101, v100, v98 offset0:128 offset1:132

	.amdhsa_kernel _Z10qkv_kernelPKfS0_S0_PKdPKtS0_PhPfS6_
		.amdhsa_group_segment_fixed_size 0
		.amdhsa_private_segment_fixed_size 0
		.amdhsa_kernarg_size 72
		.amdhsa_user_sgpr_count 2
		.amdhsa_user_sgpr_dispatch_ptr 0
		.amdhsa_user_sgpr_queue_ptr 0
		.amdhsa_user_sgpr_kernarg_segment_ptr 1
		.amdhsa_user_sgpr_dispatch_id 0
		.amdhsa_user_sgpr_kernarg_preload_length 0
		.amdhsa_user_sgpr_kernarg_preload_offset 0
		.amdhsa_user_sgpr_private_segment_size 0
		.amdhsa_uses_dynamic_stack 0
		.amdhsa_enable_private_segment 0
		.amdhsa_system_sgpr_workgroup_id_x 1
		.amdhsa_system_sgpr_workgroup_id_y 0
		.amdhsa_system_sgpr_workgroup_id_z 0
		.amdhsa_system_sgpr_workgroup_info 0
		.amdhsa_system_vgpr_workitem_id 0
		.amdhsa_next_free_vgpr 192
		.amdhsa_next_free_sgpr 32
		.amdhsa_accum_offset 192
		.amdhsa_reserve_vcc 1
		.amdhsa_float_round_mode_32 0
		.amdhsa_float_round_mode_16_64 0
		.amdhsa_float_denorm_mode_32 3
		.amdhsa_float_denorm_mode_16_64 3
		.amdhsa_dx10_clamp 1
		.amdhsa_ieee_mode 1
		.amdhsa_fp16_overflow 0
		.amdhsa_tg_split 0
		.amdhsa_exception_fp_ieee_invalid_op 0
		.amdhsa_exception_fp_denorm_src 0
		.amdhsa_exception_fp_ieee_div_zero 0
		.amdhsa_exception_fp_ieee_overflow 0
		.amdhsa_exception_fp_ieee_underflow 0
		.amdhsa_exception_fp_ieee_inexact 0
		.amdhsa_exception_int_div_zero 0
	.end_amdhsa_kernel

_Z14outproj_kernelPKhPKfS2_PKtS2_S2_Pf:
	s_bfe_u32 s18, s2, 0x20001
	s_and_b32 s19, s2, 1
	s_lshr_b32 s2, s2, 3
	s_lshl_b32 s18, s18, 7
	s_lshl_b32 s19, s19, 6
	s_or_b32 s2, s2, s18
	s_or_b32 s2, s2, s19
	s_load_dwordx2 s[12:13], s[0:1], 0x0
	s_load_dwordx8 s[4:11], s[0:1], 0x18
	v_lshrrev_b32_e32 v32, 6, v0
	v_and_b32_e32 v4, 63, v0
	v_lshlrev_b32_e32 v76, 14, v32
	v_mov_b32_e32 v77, 0
	s_waitcnt lgkmcnt(0)
	v_lshl_add_u64 v[2:3], s[4:5], 0, v[76:77]
	v_lshlrev_b32_e32 v76, 4, v4
	v_lshl_add_u64 v[6:7], v[2:3], 0, v[76:77]
	s_movk_i32 s14, 0x1000
	v_add_co_u32_e32 v98, vcc, s14, v6
	s_movk_i32 s4, 0x2000
	s_nop 0
	v_addc_co_u32_e32 v99, vcc, 0, v7, vcc
	s_ashr_i32 s16, s2, 7
	v_add_co_u32_e32 v28, vcc, s4, v6
	s_lshl_b32 s2, s2, 5
	s_ashr_i32 s17, s16, 31
	v_addc_co_u32_e32 v29, vcc, 0, v7, vcc
	s_movk_i32 s4, 0x3000
	s_and_b32 s2, s2, 0xfe0
	v_add_co_u32_e32 v100, vcc, s4, v6
	s_lshl_b64 s[4:5], s[16:17], 12
	global_load_dwordx4 v[2:5], v[6:7], off
	global_load_dwordx4 v[24:27], v[6:7], off offset:1024
	global_load_dwordx4 v[20:23], v[6:7], off offset:2048
	global_load_dwordx4 v[16:19], v[6:7], off offset:3072
	s_or_b32 s4, s4, s2
	v_lshrrev_b32_e32 v96, 5, v0
	v_lshlrev_b32_e32 v6, 3, v0
	v_addc_co_u32_e32 v101, vcc, 0, v7, vcc
	v_and_b32_e32 v10, 0xf8, v6
	v_or_b32_e32 v6, s4, v96
	v_mov_b32_e32 v7, s5
	v_mov_b32_e32 v11, v77
	v_lshl_add_u64 v[8:9], s[12:13], 0, v[10:11]
	v_lshlrev_b64 v[6:7], 8, v[6:7]
	v_lshl_add_u64 v[12:13], v[8:9], 0, v[6:7]
	s_mov_b32 s12, 0x401000
	v_add_co_u32_e32 v30, vcc, s12, v12
	v_bfe_u32 v11, v0, 5, 1
	s_nop 0
	v_addc_co_u32_e32 v31, vcc, 0, v13, vcc
	v_and_b32_e32 v1, 31, v0
	v_add_co_u32_e32 v14, vcc, s14, v12
	s_lshl_b64 s[12:13], s[16:17], 8
	v_lshlrev_b32_e32 v94, 5, v32
	v_lshlrev_b32_e32 v95, 2, v11
	v_addc_co_u32_e32 v15, vcc, 0, v13, vcc
	global_load_dwordx2 v[8:9], v[12:13], off
	global_load_dwordx2 v[6:7], v[14:15], off
	v_lshlrev_b32_e32 v76, 2, v1
	v_or3_b32 v14, s12, v94, v95
	s_mov_b32 s3, 0
	v_lshl_add_u64 v[12:13], s[8:9], 0, v[76:77]
	s_lshl_b32 s2, s2, 2
	v_mov_b32_e32 v15, s13
	v_or_b32_e32 v40, 8, v14
	v_mov_b32_e32 v41, s13
	v_lshl_add_u64 v[12:13], v[12:13], 0, s[2:3]
	v_lshlrev_b64 v[32:33], 14, v[14:15]
	v_or_b32_e32 v34, 1, v14
	v_mov_b32_e32 v35, s13
	v_or_b32_e32 v36, 2, v14
	v_mov_b32_e32 v37, s13
	v_or_b32_e32 v38, 3, v14
	v_mov_b32_e32 v39, s13
	v_lshlrev_b64 v[40:41], 14, v[40:41]
	v_or_b32_e32 v42, 9, v14
	v_mov_b32_e32 v43, s13
	v_or_b32_e32 v44, 10, v14
	v_mov_b32_e32 v45, s13
	v_or_b32_e32 v46, 11, v14
	v_mov_b32_e32 v47, s13
	v_lshl_add_u64 v[32:33], v[12:13], 0, v[32:33]
	v_lshlrev_b64 v[34:35], 14, v[34:35]
	v_lshlrev_b64 v[36:37], 14, v[36:37]
	v_lshlrev_b64 v[38:39], 14, v[38:39]
	v_lshl_add_u64 v[40:41], v[12:13], 0, v[40:41]
	v_lshlrev_b64 v[42:43], 14, v[42:43]
	v_lshlrev_b64 v[44:45], 14, v[44:45]
	v_lshlrev_b64 v[46:47], 14, v[46:47]
	v_lshl_add_u64 v[34:35], v[12:13], 0, v[34:35]
	v_lshl_add_u64 v[36:37], v[12:13], 0, v[36:37]
	v_lshl_add_u64 v[38:39], v[12:13], 0, v[38:39]
	v_lshl_add_u64 v[42:43], v[12:13], 0, v[42:43]
	v_lshl_add_u64 v[44:45], v[12:13], 0, v[44:45]
	v_lshl_add_u64 v[46:47], v[12:13], 0, v[46:47]
	global_load_dword v88, v[32:33], off
	global_load_dword v87, v[34:35], off
	global_load_dword v85, v[36:37], off
	global_load_dword v83, v[38:39], off
	global_load_dword v81, v[40:41], off
	global_load_dword v80, v[42:43], off
	global_load_dword v79, v[44:45], off
	global_load_dword v78, v[46:47], off
	v_or_b32_e32 v40, 24, v14
	v_mov_b32_e32 v41, s13
	v_lshlrev_b64 v[40:41], 14, v[40:41]
	v_lshl_add_u64 v[44:45], v[12:13], 0, v[40:41]
	v_or_b32_e32 v40, 25, v14
	v_mov_b32_e32 v41, s13
	v_lshlrev_b64 v[40:41], 14, v[40:41]
	v_or_b32_e32 v32, 16, v14
	v_mov_b32_e32 v33, s13
	v_or_b32_e32 v34, 17, v14
	v_mov_b32_e32 v35, s13
	v_or_b32_e32 v36, 18, v14
	v_mov_b32_e32 v37, s13
	v_or_b32_e32 v38, 19, v14
	v_mov_b32_e32 v39, s13
	v_lshl_add_u64 v[46:47], v[12:13], 0, v[40:41]
	v_or_b32_e32 v40, 26, v14
	v_mov_b32_e32 v41, s13
	v_or_b32_e32 v14, 27, v14
	v_lshlrev_b64 v[32:33], 14, v[32:33]
	v_lshlrev_b64 v[34:35], 14, v[34:35]
	v_lshlrev_b64 v[36:37], 14, v[36:37]
	v_lshlrev_b64 v[38:39], 14, v[38:39]
	v_lshlrev_b64 v[40:41], 14, v[40:41]
	v_lshlrev_b64 v[14:15], 14, v[14:15]
	v_lshl_add_u64 v[32:33], v[12:13], 0, v[32:33]
	v_lshl_add_u64 v[34:35], v[12:13], 0, v[34:35]
	v_lshl_add_u64 v[36:37], v[12:13], 0, v[36:37]
	v_lshl_add_u64 v[38:39], v[12:13], 0, v[38:39]
	v_lshl_add_u64 v[64:65], v[12:13], 0, v[40:41]
	v_lshl_add_u64 v[66:67], v[12:13], 0, v[14:15]
	global_load_dwordx2 v[14:15], v[30:31], off offset:-4096
	global_load_dwordx2 v[12:13], v[30:31], off
	global_load_dword v93, v[32:33], off
	global_load_dword v92, v[34:35], off
	global_load_dword v91, v[36:37], off
	global_load_dword v90, v[38:39], off
	global_load_dword v89, v[44:45], off
	global_load_dword v86, v[46:47], off
	global_load_dword v84, v[64:65], off
	global_load_dword v82, v[66:67], off
	global_load_dwordx4 v[60:63], v[28:29], off offset:-4096
	global_load_dwordx4 v[56:59], v[28:29], off
	global_load_dwordx4 v[52:55], v[28:29], off offset:1024
	global_load_dwordx4 v[48:51], v[28:29], off offset:2048
	global_load_dwordx4 v[40:43], v[28:29], off offset:3072
	global_load_dwordx4 v[72:75], v[98:99], off offset:1024
	global_load_dwordx4 v[68:71], v[98:99], off offset:2048
	global_load_dwordx4 v[64:67], v[98:99], off offset:3072
	global_load_dwordx4 v[44:47], v[100:101], off
	global_load_dwordx4 v[36:39], v[100:101], off offset:1024
	global_load_dwordx4 v[32:35], v[100:101], off offset:2048
	global_load_dwordx4 v[28:31], v[100:101], off offset:3072
	v_cmp_gt_u32_e32 vcc, 32, v0
	s_and_saveexec_b64 s[8:9], vcc
	s_cbranch_execz .LBB3_2
	s_load_dwordx4 s[12:15], s[0:1], 0x8
	s_add_u32 s0, s4, 0x4000
	s_addc_u32 s1, s5, 0
	v_or_b32_e32 v102, s0, v0
	v_mov_b32_e32 v103, s1
	v_or_b32_e32 v98, s4, v0
	v_mov_b32_e32 v99, s5
	v_lshlrev_b64 v[102:103], 2, v[102:103]
	v_lshlrev_b64 v[98:99], 2, v[98:99]
	s_waitcnt lgkmcnt(0)
	v_lshl_add_u64 v[104:105], s[14:15], 0, v[102:103]
	v_lshl_add_u64 v[100:101], s[14:15], 0, v[98:99]
	global_load_dword v97, v[104:105], off
	global_load_dword v106, v[100:101], off
	v_lshl_add_u64 v[98:99], s[12:13], 0, v[98:99]
	v_lshl_add_u64 v[100:101], s[12:13], 0, v[102:103]
	global_load_dword v102, v[98:99], off
	global_load_dword v103, v[100:101], off
	v_lshlrev_b32_e32 v104, 2, v0
	s_waitcnt vmcnt(3)
	v_max_f32_e32 v98, v97, v97
	s_waitcnt vmcnt(2)
	v_max_f32_e32 v99, v106, v106
	v_max_f32_e32 v98, v99, v98
	v_sub_f32_e32 v99, v106, v98
	v_sub_f32_e32 v97, v97, v98
	v_exp_f32_e32 v98, v99
	v_exp_f32_e32 v97, v97
	s_nop 0
	v_add_f32_e32 v99, v98, v97
	v_div_scale_f32 v100, s[0:1], v99, v99, 1.0
	v_rcp_f32_e32 v101, v100
	v_div_scale_f32 v105, vcc, 1.0, v99, 1.0
	v_fma_f32 v106, -v100, v101, 1.0
	v_fmac_f32_e32 v101, v106, v101
	v_mul_f32_e32 v106, v105, v101
	v_fma_f32 v107, -v100, v106, v105
	v_fmac_f32_e32 v106, v107, v101
	v_fma_f32 v100, -v100, v106, v105
	v_div_fmas_f32 v100, v100, v101, v106
	v_div_fixup_f32 v99, v100, v99, 1.0
	v_mul_f32_e32 v98, v98, v99
	v_mul_f32_e32 v97, v97, v99
	s_waitcnt vmcnt(1)
	v_mul_f32_e32 v98, v102, v98
	s_waitcnt vmcnt(0)
	v_mul_f32_e32 v97, v103, v97
	v_add_u32_e32 v99, 0x4000, v104
	ds_write2_b32 v99, v98, v97 offset1:32

	.amdhsa_kernel _Z14outproj_kernelPKhPKfS2_PKtS2_S2_Pf
		.amdhsa_group_segment_fixed_size 16640
		.amdhsa_private_segment_fixed_size 0
		.amdhsa_kernarg_size 56
		.amdhsa_user_sgpr_count 2
		.amdhsa_user_sgpr_dispatch_ptr 0
		.amdhsa_user_sgpr_queue_ptr 0
		.amdhsa_user_sgpr_kernarg_segment_ptr 1
		.amdhsa_user_sgpr_dispatch_id 0
		.amdhsa_user_sgpr_kernarg_preload_length 0
		.amdhsa_user_sgpr_kernarg_preload_offset 0
		.amdhsa_user_sgpr_private_segment_size 0
		.amdhsa_uses_dynamic_stack 0
		.amdhsa_enable_private_segment 0
		.amdhsa_system_sgpr_workgroup_id_x 1
		.amdhsa_system_sgpr_workgroup_id_y 0
		.amdhsa_system_sgpr_workgroup_id_z 0
		.amdhsa_system_sgpr_workgroup_info 0
		.amdhsa_system_vgpr_workitem_id 0
		.amdhsa_next_free_vgpr 109
		.amdhsa_next_free_sgpr 20
		.amdhsa_accum_offset 112
		.amdhsa_reserve_vcc 1
		.amdhsa_float_round_mode_32 0
		.amdhsa_float_round_mode_16_64 0
		.amdhsa_float_denorm_mode_32 3
		.amdhsa_float_denorm_mode_16_64 3
		.amdhsa_dx10_clamp 1
		.amdhsa_ieee_mode 1
		.amdhsa_fp16_overflow 0
		.amdhsa_tg_split 0
		.amdhsa_exception_fp_ieee_invalid_op 0
		.amdhsa_exception_fp_denorm_src 0
		.amdhsa_exception_fp_ieee_div_zero 0
		.amdhsa_exception_fp_ieee_overflow 0
		.amdhsa_exception_fp_ieee_underflow 0
		.amdhsa_exception_fp_ieee_inexact 0
		.amdhsa_exception_int_div_zero 0
	.end_amdhsa_kernel

amdhsa.kernels:
  - .agpr_count:     0
    .args:
      - .actual_access:  read_only
        .address_space:  global
        .offset:         0
        .size:           8
        .value_kind:     global_buffer
      - .actual_access:  read_only
        .address_space:  global
        .offset:         8
        .size:           8
        .value_kind:     global_buffer
      - .actual_access:  read_only
        .address_space:  global
        .offset:         16
        .size:           8
        .value_kind:     global_buffer
      - .actual_access:  write_only
        .address_space:  global
        .offset:         24
        .size:           8
        .value_kind:     global_buffer
      - .actual_access:  write_only
        .address_space:  global
        .offset:         32
        .size:           8
        .value_kind:     global_buffer
      - .actual_access:  write_only
        .address_space:  global
        .offset:         40
        .size:           8
        .value_kind:     global_buffer
    .group_segment_fixed_size: 512
    .kernarg_segment_align: 8
    .kernarg_segment_size: 48
    .language:       OpenCL C
    .language_version:
      - 2
      - 0
    .max_flat_workgroup_size: 1024
    .name:           _Z11prep_kernelPKfS0_S0_PdPtS2_
    .private_segment_fixed_size: 0
    .sgpr_count:     26
    .sgpr_spill_count: 0
    .symbol:         _Z11prep_kernelPKfS0_S0_PdPtS2_.kd
    .uniform_work_group_size: 1
    .uses_dynamic_stack: false
    .vgpr_count:     32
    .vgpr_spill_count: 0
    .wavefront_size: 64
  - .agpr_count:     0
    .args:
      - .actual_access:  read_only
        .address_space:  global
        .offset:         0
        .size:           8
        .value_kind:     global_buffer
      - .actual_access:  read_only
        .address_space:  global
        .offset:         8
        .size:           8
        .value_kind:     global_buffer
      - .actual_access:  read_only
        .address_space:  global
        .offset:         16
        .size:           8
        .value_kind:     global_buffer
      - .actual_access:  read_only
        .address_space:  global
        .offset:         24
        .size:           8
        .value_kind:     global_buffer
      - .actual_access:  read_only
        .address_space:  global
        .offset:         32
        .size:           8
        .value_kind:     global_buffer
      - .actual_access:  read_only
        .address_space:  global
        .offset:         40
        .size:           8
        .value_kind:     global_buffer
      - .actual_access:  write_only
        .address_space:  global
        .offset:         48
        .size:           8
        .value_kind:     global_buffer
      - .actual_access:  write_only
        .address_space:  global
        .offset:         56
        .size:           8
        .value_kind:     global_buffer
      - .actual_access:  write_only
        .address_space:  global
        .offset:         64
        .size:           8
        .value_kind:     global_buffer
    .group_segment_fixed_size: 0
    .kernarg_segment_align: 8
    .kernarg_segment_size: 72
    .language:       OpenCL C
    .language_version:
      - 2
      - 0
    .max_flat_workgroup_size: 512
    .name:           _Z10qkv_kernelPKfS0_S0_PKdPKtS0_PhPfS6_
    .private_segment_fixed_size: 0
    .sgpr_count:     38
    .sgpr_spill_count: 0
    .symbol:         _Z10qkv_kernelPKfS0_S0_PKdPKtS0_PhPfS6_.kd
    .uniform_work_group_size: 1
    .uses_dynamic_stack: false
    .vgpr_count:     192
    .vgpr_spill_count: 0
    .wavefront_size: 64
  - .agpr_count:     0
    .args:
      - .actual_access:  read_only
        .address_space:  global
        .offset:         0
        .size:           8
        .value_kind:     global_buffer
      - .address_space:  global
        .offset:         8
        .size:           8
        .value_kind:     global_buffer
      - .address_space:  global
        .offset:         16
        .size:           8
        .value_kind:     global_buffer
      - .actual_access:  read_only
        .address_space:  global
        .offset:         24
        .size:           8
        .value_kind:     global_buffer
      - .actual_access:  read_only
        .address_space:  global
        .offset:         32
        .size:           8
        .value_kind:     global_buffer
      - .actual_access:  write_only
        .address_space:  global
        .offset:         40
        .size:           8
        .value_kind:     global_buffer
      - .actual_access:  write_only
        .address_space:  global
        .offset:         48
        .size:           8
        .value_kind:     global_buffer
      - .actual_access:  write_only
        .address_space:  global
        .offset:         56
        .size:           8
        .value_kind:     global_buffer
    .group_segment_fixed_size: 0
    .kernarg_segment_align: 8
    .kernarg_segment_size: 64
    .language:       OpenCL C
    .language_version:
      - 2
      - 0
    .max_flat_workgroup_size: 512
    .name:           _Z11attn_kernelPKhS0_S0_PKfS2_PhPfS4_
    .private_segment_fixed_size: 0
    .sgpr_count:     72
    .sgpr_spill_count: 0
    .symbol:         _Z11attn_kernelPKhS0_S0_PKfS2_PhPfS4_.kd
    .uniform_work_group_size: 1
    .uses_dynamic_stack: false
    .vgpr_count:     256
    .vgpr_spill_count: 0
    .wavefront_size: 64
  - .agpr_count:     0
    .args:
      - .actual_access:  read_only
        .address_space:  global
        .offset:         0
        .size:           8
        .value_kind:     global_buffer
      - .actual_access:  read_only
        .address_space:  global
        .offset:         8
        .size:           8
        .value_kind:     global_buffer
      - .actual_access:  read_only
        .address_space:  global
        .offset:         16
        .size:           8
        .value_kind:     global_buffer
      - .actual_access:  read_only
        .address_space:  global
        .offset:         24
        .size:           8
        .value_kind:     global_buffer
      - .actual_access:  read_only
        .address_space:  global
        .offset:         32
        .size:           8
        .value_kind:     global_buffer
      - .actual_access:  read_only
        .address_space:  global
        .offset:         40
        .size:           8
        .value_kind:     global_buffer
      - .actual_access:  write_only
        .address_space:  global
        .offset:         48
        .size:           8
        .value_kind:     global_buffer
    .group_segment_fixed_size: 16640
    .kernarg_segment_align: 8
    .kernarg_segment_size: 56
    .language:       OpenCL C
    .language_version:
      - 2
      - 0
    .max_flat_workgroup_size: 512
    .name:           _Z14outproj_kernelPKhPKfS2_PKtS2_S2_Pf
    .private_segment_fixed_size: 0
    .sgpr_count:     26
    .sgpr_spill_count: 0
    .symbol:         _Z14outproj_kernelPKhPKfS2_PKtS2_S2_Pf.kd
    .uniform_work_group_size: 1
    .uses_dynamic_stack: false
    .vgpr_count:     109
    .vgpr_spill_count: 0
    .wavefront_size: 64
